# grid barrier: invalidate issued at arrival and not waited for before the leader decision (counted vmcnt)
# baseline (speedup 1.0000x reference)
; __device__ __forceinline__ unsigned xb_add(unsigned* p, unsigned v) { return __hip_atomic_fetch_add(p, v, __ATOMIC_RELAXED, __HIP_MEMORY_SCOPE_AGENT); }
; __device__ __forceinline__ void xcd_barrier(const XcdBarrier& b) {
;     ...
;         const unsigned old = xb_add(&bar[XB_XSUB(b.x)], 1u);
;         const unsigned gen = old / nloc;
;         if (old + 1u == (gen + 1u) * nloc) {
.LBB0_266:
	v_readlane_b32 s4, v247, 7
	s_lshl_b32 s4, s4, 8
	s_add_u32 s4, s72, s4
	s_addc_u32 s5, s73, 0
	v_mov_b32_e32 v2, 0x1000
	v_mov_b32_e32 v4, 1
	global_atomic_add v4, v2, v4, s[4:5] offset:1024 sc0
	buffer_inv sc1
	v_cvt_f32_u32_e32 v2, v3
	v_sub_u32_e32 v5, 0, v3
	v_rcp_iflag_f32_e32 v2, v2
	s_nop 0
	v_mul_f32_e32 v2, 0x4f7ffffe, v2
	v_cvt_u32_f32_e32 v2, v2
	v_mul_lo_u32 v5, v5, v2
	v_mul_hi_u32 v5, v2, v5
	v_add_u32_e32 v2, v2, v5
	s_waitcnt vmcnt(1)
	v_mul_hi_u32 v2, v4, v2
	v_mul_lo_u32 v5, v2, v3
	v_sub_u32_e32 v5, v4, v5
	v_add_u32_e32 v6, 1, v2
	v_cmp_ge_u32_e32 vcc, v5, v3
	v_add_u32_e32 v4, 1, v4
	s_nop 0
	v_cndmask_b32_e32 v2, v2, v6, vcc
	v_sub_u32_e32 v6, v5, v3
	v_cndmask_b32_e32 v5, v5, v6, vcc
	v_add_u32_e32 v6, 1, v2
	v_cmp_ge_u32_e32 vcc, v5, v3
	s_nop 1
	v_cndmask_b32_e32 v2, v2, v6, vcc
	v_mul_lo_u32 v5, v3, v2
	v_add_u32_e32 v3, v5, v3
	v_cmp_ne_u32_e32 vcc, v4, v3
	s_and_saveexec_b64 s[6:7], vcc
	s_xor_b64 s[6:7], exec, s[6:7]
	s_cbranch_execz .LBB0_280
	s_waitcnt lgkmcnt(0)
	v_mov_b32_e32 v1, 0x2000
	global_load_dword v1, v1, s[4:5] offset:1024 sc1
	s_add_u32 s12, s4, 0x2400
	s_addc_u32 s13, s5, 0
	s_waitcnt vmcnt(0)
	v_cmp_eq_u32_e32 vcc, v1, v2
	s_and_saveexec_b64 s[8:9], vcc
	s_cbranch_execz .LBB0_279
	s_add_u32 s10, s86, 0x4200
	s_addc_u32 s11, s87, 0
	s_mov_b32 s24, 1
	s_mov_b64 s[14:15], 0
	v_mov_b32_e32 v1, 0
	s_branch .LBB0_270

; __device__ __forceinline__ unsigned xb_add(unsigned* p, unsigned v) { return __hip_atomic_fetch_add(p, v, __ATOMIC_RELAXED, __HIP_MEMORY_SCOPE_AGENT); }
; __device__ __forceinline__ void xcd_barrier(const XcdBarrier& b) {
;     ...
;         const unsigned old = xb_add(&bar[XB_XSUB(b.x)], 1u);
;         const unsigned gen = old / nloc;
;         if (old + 1u == (gen + 1u) * nloc) {
.LBB0_696:
	v_readlane_b32 s4, v247, 7
	s_lshl_b32 s4, s4, 8
	s_add_u32 s4, s72, s4
	s_addc_u32 s5, s73, 0
	v_mov_b32_e32 v3, 0x1000
	v_mov_b32_e32 v5, 1
	global_atomic_add v5, v3, v5, s[4:5] offset:1024 sc0
	buffer_inv sc1
	v_cvt_f32_u32_e32 v3, v4
	v_sub_u32_e32 v6, 0, v4
	v_rcp_iflag_f32_e32 v3, v3
	s_nop 0
	v_mul_f32_e32 v3, 0x4f7ffffe, v3
	v_cvt_u32_f32_e32 v3, v3
	v_mul_lo_u32 v6, v6, v3
	v_mul_hi_u32 v6, v3, v6
	v_add_u32_e32 v3, v3, v6
	s_waitcnt vmcnt(1)
	v_mul_hi_u32 v3, v5, v3
	v_mul_lo_u32 v6, v3, v4
	v_sub_u32_e32 v6, v5, v6
	v_add_u32_e32 v7, 1, v3
	v_cmp_ge_u32_e32 vcc, v6, v4
	v_add_u32_e32 v5, 1, v5
	s_nop 0
	v_cndmask_b32_e32 v3, v3, v7, vcc
	v_sub_u32_e32 v7, v6, v4
	v_cndmask_b32_e32 v6, v6, v7, vcc
	v_add_u32_e32 v7, 1, v3
	v_cmp_ge_u32_e32 vcc, v6, v4
	s_nop 1
	v_cndmask_b32_e32 v3, v3, v7, vcc
	v_mul_lo_u32 v6, v4, v3
	v_add_u32_e32 v4, v6, v4
	v_cmp_ne_u32_e32 vcc, v5, v4
	s_and_saveexec_b64 s[6:7], vcc
	s_xor_b64 s[6:7], exec, s[6:7]
	s_cbranch_execz .LBB0_710
	s_waitcnt lgkmcnt(0)
	v_mov_b32_e32 v2, 0x2000
	global_load_dword v2, v2, s[4:5] offset:1024 sc1
	s_add_u32 s12, s4, 0x2400
	s_addc_u32 s13, s5, 0
	s_waitcnt vmcnt(0)
	v_cmp_eq_u32_e32 vcc, v2, v3
	s_and_saveexec_b64 s[8:9], vcc
	s_cbranch_execz .LBB0_709
	s_add_u32 s10, s86, 0x4200
	s_addc_u32 s11, s87, 0
	s_mov_b32 s24, 1
	s_mov_b64 s[14:15], 0
	v_mov_b32_e32 v2, 0
	s_branch .LBB0_700

; __device__ __forceinline__ unsigned xb_add(unsigned* p, unsigned v) { return __hip_atomic_fetch_add(p, v, __ATOMIC_RELAXED, __HIP_MEMORY_SCOPE_AGENT); }
; __device__ __forceinline__ void xcd_barrier(const XcdBarrier& b) {
;     ...
;         const unsigned old = xb_add(&bar[XB_XSUB(b.x)], 1u);
;         const unsigned gen = old / nloc;
;         if (old + 1u == (gen + 1u) * nloc) {
.LBB0_1742:
	v_readlane_b32 s4, v247, 7
	s_lshl_b32 s4, s4, 8
	s_add_u32 s4, s72, s4
	s_addc_u32 s5, s73, 0
	v_mov_b32_e32 v2, 0x1000
	v_mov_b32_e32 v4, 1
	global_atomic_add v4, v2, v4, s[4:5] offset:1024 sc0
	buffer_inv sc1
	v_cvt_f32_u32_e32 v2, v3
	v_sub_u32_e32 v5, 0, v3
	v_rcp_iflag_f32_e32 v2, v2
	s_nop 0
	v_mul_f32_e32 v2, 0x4f7ffffe, v2
	v_cvt_u32_f32_e32 v2, v2
	v_mul_lo_u32 v5, v5, v2
	v_mul_hi_u32 v5, v2, v5
	v_add_u32_e32 v2, v2, v5
	s_waitcnt vmcnt(1)
	v_mul_hi_u32 v2, v4, v2
	v_mul_lo_u32 v5, v2, v3
	v_sub_u32_e32 v5, v4, v5
	v_add_u32_e32 v6, 1, v2
	v_cmp_ge_u32_e32 vcc, v5, v3
	v_add_u32_e32 v4, 1, v4
	s_nop 0
	v_cndmask_b32_e32 v2, v2, v6, vcc
	v_sub_u32_e32 v6, v5, v3
	v_cndmask_b32_e32 v5, v5, v6, vcc
	v_add_u32_e32 v6, 1, v2
	v_cmp_ge_u32_e32 vcc, v5, v3
	s_nop 1
	v_cndmask_b32_e32 v2, v2, v6, vcc
	v_mul_lo_u32 v5, v3, v2
	v_add_u32_e32 v3, v5, v3
	v_cmp_ne_u32_e32 vcc, v4, v3
	s_and_saveexec_b64 s[6:7], vcc
	s_xor_b64 s[6:7], exec, s[6:7]
	s_cbranch_execz .LBB0_1756
	s_waitcnt lgkmcnt(0)
	v_mov_b32_e32 v1, 0x2000
	global_load_dword v1, v1, s[4:5] offset:1024 sc1
	s_add_u32 s14, s4, 0x2400
	s_addc_u32 s15, s5, 0
	s_waitcnt vmcnt(0)
	v_cmp_eq_u32_e32 vcc, v1, v2
	s_and_saveexec_b64 s[10:11], vcc
	s_cbranch_execz .LBB0_1755
	s_add_u32 s12, s86, 0x4200
	s_addc_u32 s13, s87, 0
	s_mov_b32 s26, 1
	s_mov_b64 s[16:17], 0
	v_mov_b32_e32 v1, 0
	s_branch .LBB0_1746

; __device__ __forceinline__ unsigned xb_add(unsigned* p, unsigned v) { return __hip_atomic_fetch_add(p, v, __ATOMIC_RELAXED, __HIP_MEMORY_SCOPE_AGENT); }
; __device__ __forceinline__ void xcd_barrier(const XcdBarrier& b) {
;     ...
;         const unsigned old = xb_add(&bar[XB_XSUB(b.x)], 1u);
;         const unsigned gen = old / nloc;
;         if (old + 1u == (gen + 1u) * nloc) {
.LBB0_2077:
	v_readlane_b32 s0, v247, 7
	s_lshl_b32 s0, s0, 8
	s_add_u32 s0, s72, s0
	s_addc_u32 s1, s73, 0
	v_mov_b32_e32 v3, 0x1000
	v_mov_b32_e32 v5, 1
	global_atomic_add v5, v3, v5, s[0:1] offset:1024 sc0
	buffer_inv sc1
	v_cvt_f32_u32_e32 v3, v4
	v_sub_u32_e32 v6, 0, v4
	v_rcp_iflag_f32_e32 v3, v3
	s_nop 0
	v_mul_f32_e32 v3, 0x4f7ffffe, v3
	v_cvt_u32_f32_e32 v3, v3
	v_mul_lo_u32 v6, v6, v3
	v_mul_hi_u32 v6, v3, v6
	v_add_u32_e32 v3, v3, v6
	s_waitcnt vmcnt(1)
	v_mul_hi_u32 v3, v5, v3
	v_mul_lo_u32 v6, v3, v4
	v_sub_u32_e32 v6, v5, v6
	v_add_u32_e32 v7, 1, v3
	v_cmp_ge_u32_e32 vcc, v6, v4
	v_add_u32_e32 v5, 1, v5
	s_nop 0
	v_cndmask_b32_e32 v3, v3, v7, vcc
	v_sub_u32_e32 v7, v6, v4
	v_cndmask_b32_e32 v6, v6, v7, vcc
	v_add_u32_e32 v7, 1, v3
	v_cmp_ge_u32_e32 vcc, v6, v4
	s_nop 1
	v_cndmask_b32_e32 v3, v3, v7, vcc
	v_mul_lo_u32 v6, v4, v3
	v_add_u32_e32 v4, v6, v4
	v_cmp_ne_u32_e32 vcc, v5, v4
	s_and_saveexec_b64 s[4:5], vcc
	s_xor_b64 s[4:5], exec, s[4:5]
	s_cbranch_execz .LBB0_2091
	s_waitcnt lgkmcnt(0)
	v_mov_b32_e32 v2, 0x2000
	global_load_dword v2, v2, s[0:1] offset:1024 sc1
	s_add_u32 s14, s0, 0x2400
	s_addc_u32 s15, s1, 0
	s_waitcnt vmcnt(0)
	v_cmp_eq_u32_e32 vcc, v2, v3
	s_and_saveexec_b64 s[6:7], vcc
	s_cbranch_execz .LBB0_2090
	s_add_u32 s12, s86, 0x4200
	s_addc_u32 s13, s87, 0
	s_mov_b32 s26, 1
	s_mov_b64 s[16:17], 0
	v_mov_b32_e32 v2, 0
	s_branch .LBB0_2081

; __device__ __forceinline__ unsigned xb_add(unsigned* p, unsigned v) { return __hip_atomic_fetch_add(p, v, __ATOMIC_RELAXED, __HIP_MEMORY_SCOPE_AGENT); }
; __device__ __forceinline__ void xcd_barrier(const XcdBarrier& b) {
;     ...
;         const unsigned old = xb_add(&bar[XB_XSUB(b.x)], 1u);
;         const unsigned gen = old / nloc;
;         if (old + 1u == (gen + 1u) * nloc) {
.LBB0_2157:
	v_readlane_b32 s4, v247, 7
	s_lshl_b32 s4, s4, 8
	s_add_u32 s4, s72, s4
	s_addc_u32 s5, s73, 0
	v_mov_b32_e32 v1, 0x1000
	v_mov_b32_e32 v3, 1
	global_atomic_add v3, v1, v3, s[4:5] offset:1024 sc0
	buffer_inv sc1
	v_cvt_f32_u32_e32 v1, v2
	v_sub_u32_e32 v4, 0, v2
	v_rcp_iflag_f32_e32 v1, v1
	s_nop 0
	v_mul_f32_e32 v1, 0x4f7ffffe, v1
	v_cvt_u32_f32_e32 v1, v1
	v_mul_lo_u32 v4, v4, v1
	v_mul_hi_u32 v4, v1, v4
	v_add_u32_e32 v1, v1, v4
	s_waitcnt vmcnt(1)
	v_mul_hi_u32 v1, v3, v1
	v_mul_lo_u32 v4, v1, v2
	v_sub_u32_e32 v4, v3, v4
	v_add_u32_e32 v5, 1, v1
	v_cmp_ge_u32_e32 vcc, v4, v2
	v_add_u32_e32 v3, 1, v3
	s_nop 0
	v_cndmask_b32_e32 v1, v1, v5, vcc
	v_sub_u32_e32 v5, v4, v2
	v_cndmask_b32_e32 v4, v4, v5, vcc
	v_add_u32_e32 v5, 1, v1
	v_cmp_ge_u32_e32 vcc, v4, v2
	s_nop 1
	v_cndmask_b32_e32 v1, v1, v5, vcc
	v_mul_lo_u32 v4, v2, v1
	v_add_u32_e32 v2, v4, v2
	v_cmp_ne_u32_e32 vcc, v3, v2
	s_and_saveexec_b64 s[6:7], vcc
	s_xor_b64 s[6:7], exec, s[6:7]
	s_cbranch_execz .LBB0_2171
	s_waitcnt lgkmcnt(0)
	v_mov_b32_e32 v0, 0x2000
	global_load_dword v0, v0, s[4:5] offset:1024 sc1
	s_add_u32 s14, s4, 0x2400
	s_addc_u32 s15, s5, 0
	s_waitcnt vmcnt(0)
	v_cmp_eq_u32_e32 vcc, v0, v1
	s_and_saveexec_b64 s[10:11], vcc
	s_cbranch_execz .LBB0_2170
	s_add_u32 s12, s86, 0x4200
	s_addc_u32 s13, s87, 0
	s_mov_b32 s26, 1
	s_mov_b64 s[16:17], 0
	v_mov_b32_e32 v0, 0
	s_branch .LBB0_2161
